# v27
# baseline (speedup 1.0000x reference)
_Z12pool1_kernelPKfS0_S0_S0_S0_S0_S0_S0_S0_S0_PfS1_:
	s_load_dwordx4 s[12:15], s[0:1], 0x0
	s_load_dwordx2 s[36:37], s[0:1], 0x48
	s_load_dwordx2 s[38:39], s[0:1], 0x58
	s_load_dwordx2 s[48:49], s[0:1], 0x20
	s_load_dwordx4 s[44:47], s[0:1], 0x10
	s_cmp_eq_u32 s2, 0
	s_movk_i32 s3, 0x80
	s_cselect_b64 s[4:5], -1, 0
	v_cmp_gt_u32_e64 s[10:11], s3, v0
	s_and_b64 s[6:7], s[4:5], s[10:11]
	s_and_saveexec_b64 s[4:5], s[6:7]
	s_cbranch_execz .LBB0_2
	v_mov_b32_e32 v1, 0
	v_lshlrev_b64 v[2:3], 2, v[0:1]
	s_waitcnt lgkmcnt(0)
	v_lshl_add_u64 v[4:5], s[36:37], 0, v[2:3]
	global_load_dword v253, v[4:5], off
	v_lshl_add_u64 v[254:255], s[38:39], 0, v[2:3]
.LBB0_2:
	s_or_b64 exec, exec, s[4:5]
	v_mov_b32_e32 v3, 0
	v_lshlrev_b32_e32 v130, 2, v0
	v_and_b32_e32 v131, 63, v0
	v_readfirstlane_b32 s3, v0
	v_lshlrev_b32_e32 v204, 4, v131
	v_lshlrev_b32_e32 v222, 4, v0
	v_add_u32_e32 v223, 0x2000, v222
	v_add_u32_e32 v224, 0x4000, v222
	v_add_u32_e32 v225, 0x6000, v222
	v_add_u32_e32 v226, 0x8000, v222
	v_add_u32_e32 v227, 0xa000, v222
	v_add_u32_e32 v228, 0xc000, v222
	v_add_u32_e32 v229, 0xe000, v222
	v_add_u32_e32 v230, 0x10000, v222
	v_add_u32_e32 v231, 0x12000, v222
	v_add_u32_e32 v232, 0x14000, v222
	v_add_u32_e32 v233, 0x16000, v222
	v_add_u32_e32 v234, 0x18000, v222
	v_add_u32_e32 v235, 0x1a000, v222
	v_add_u32_e32 v236, 0x1c000, v222
	v_add_u32_e32 v237, 0x1e000, v222
	v_and_b32_e32 v250, 0x7f, v0
	v_lshlrev_b32_e32 v250, 2, v250
	s_lshr_b32 s31, s3, 6
	s_lshl_b32 s33, s2, 21
	s_waitcnt lgkmcnt(0)
	s_mov_b64 s[40:41], s[14:15]
	s_load_dword s43, s[48:49], 0x0
	s_mov_b32 s15, 0x20000
	s_brev_b32 s14, -2
	s_and_b32 s13, s13, 0xffff
	global_load_dwordx4 v[4:7], v222, s[40:41]
	global_load_dwordx4 v[8:11], v223, s[40:41]
	global_load_dwordx4 v[12:15], v224, s[40:41]
	global_load_dwordx4 v[16:19], v225, s[40:41]
	global_load_dwordx4 v[20:23], v226, s[40:41]
	global_load_dwordx4 v[24:27], v227, s[40:41]
	global_load_dwordx4 v[28:31], v228, s[40:41]
	global_load_dwordx4 v[98:101], v229, s[40:41]
	global_load_dwordx4 v[102:105], v230, s[40:41]
	global_load_dwordx4 v[106:109], v231, s[40:41]
	global_load_dwordx4 v[110:113], v232, s[40:41]
	global_load_dwordx4 v[114:117], v233, s[40:41]
	global_load_dwordx4 v[118:121], v234, s[40:41]
	global_load_dwordx4 v[122:125], v235, s[40:41]
	global_load_dwordx4 v[126:129], v236, s[40:41]
	global_load_dwordx4 v[132:135], v237, s[40:41]
	global_load_dword v248, v250, s[44:45]
	global_load_dword v249, v250, s[46:47]
	s_load_dwordx2 s[20:21], s[0:1], 0x50
	s_load_dwordx2 s[22:23], s[0:1], 0x40
	s_load_dwordx2 s[4:5], s[0:1], 0x20
	s_load_dwordx4 s[16:19], s[0:1], 0x30
	s_lshl_b32 s6, s31, 14
	s_add_i32 s6, s6, s33
	s_or_b32 s7, s6, 0x1000
	buffer_load_dwordx4 v[34:37], v204, s[12:15], s6 offen sc0 nt sc1
	buffer_load_dwordx4 v[38:41], v204, s[12:15], s7 offen sc0 nt sc1
	s_or_b32 s7, s6, 0x2000
	s_or_b32 s8, s6, 0x3000
	buffer_load_dwordx4 v[42:45], v204, s[12:15], s7 offen sc0 nt sc1
	buffer_load_dwordx4 v[46:49], v204, s[12:15], s8 offen sc0 nt sc1
	s_or_b32 s7, s6, 0x400
	s_or_b32 s8, s6, 0x1400
	buffer_load_dwordx4 v[50:53], v204, s[12:15], s7 offen sc0 nt sc1
	buffer_load_dwordx4 v[54:57], v204, s[12:15], s8 offen sc0 nt sc1
	s_or_b32 s7, s6, 0x2400
	s_or_b32 s8, s6, 0x3400
	buffer_load_dwordx4 v[58:61], v204, s[12:15], s7 offen sc0 nt sc1
	buffer_load_dwordx4 v[62:65], v204, s[12:15], s8 offen sc0 nt sc1
	s_or_b32 s7, s6, 0x800
	s_or_b32 s8, s6, 0x1800
	buffer_load_dwordx4 v[66:69], v204, s[12:15], s7 offen sc0 nt sc1
	buffer_load_dwordx4 v[70:73], v204, s[12:15], s8 offen sc0 nt sc1
	s_or_b32 s7, s6, 0x2800
	s_or_b32 s8, s6, 0x3800
	buffer_load_dwordx4 v[74:77], v204, s[12:15], s7 offen sc0 nt sc1
	buffer_load_dwordx4 v[78:81], v204, s[12:15], s8 offen sc0 nt sc1
	s_or_b32 s7, s6, 0xc00
	s_or_b32 s8, s6, 0x1c00
	buffer_load_dwordx4 v[82:85], v204, s[12:15], s7 offen sc0 nt sc1
	buffer_load_dwordx4 v[86:89], v204, s[12:15], s8 offen sc0 nt sc1
	s_or_b32 s7, s6, 0x2c00
	s_or_b32 s6, s6, 0x3c00
	buffer_load_dwordx4 v[90:93], v204, s[12:15], s7 offen sc0 nt sc1
	buffer_load_dwordx4 v[94:97], v204, s[12:15], s6 offen sc0 nt sc1
	v_lshlrev_b32_e32 v2, 3, v0
	v_and_b32_e32 v1, 0x1f8, v2
	v_lshrrev_b32_e32 v32, 6, v0
	s_movk_i32 s6, 0x220
	s_waitcnt vmcnt(31)
	v_cvt_pk_bf16_f32 v4, v4, v5
	v_cvt_pk_bf16_f32 v5, v6, v7
	v_mad_u32_u24 v6, v32, s6, v1
	ds_write_b64 v6, v[4:5]
	v_add_u32_e32 v4, 0x200, v0
	v_lshrrev_b32_e32 v7, 6, v4
	s_waitcnt vmcnt(30)
	v_cvt_pk_bf16_f32 v4, v8, v9
	v_cvt_pk_bf16_f32 v5, v10, v11
	v_mad_u32_u24 v7, v7, s6, v1
	ds_write_b64 v7, v[4:5]
	s_waitcnt vmcnt(29)
	v_cvt_pk_bf16_f32 v4, v12, v13
	v_cvt_pk_bf16_f32 v5, v14, v15
	ds_write_b64 v6, v[4:5] offset:8704
	v_add_u32_e32 v4, 0x600, v0
	v_lshrrev_b32_e32 v7, 6, v4
	s_waitcnt vmcnt(28)
	v_cvt_pk_bf16_f32 v4, v16, v17
	v_cvt_pk_bf16_f32 v5, v18, v19
	v_mad_u32_u24 v7, v7, s6, v1
	ds_write_b64 v7, v[4:5]
	s_waitcnt vmcnt(27)
	v_cvt_pk_bf16_f32 v4, v20, v21
	v_cvt_pk_bf16_f32 v5, v22, v23
	ds_write_b64 v6, v[4:5] offset:17408
	v_add_u32_e32 v4, 0xa00, v0
	v_lshrrev_b32_e32 v7, 6, v4
	s_waitcnt vmcnt(26)
	v_cvt_pk_bf16_f32 v4, v24, v25
	v_cvt_pk_bf16_f32 v5, v26, v27
	v_mad_u32_u24 v7, v7, s6, v1
	ds_write_b64 v7, v[4:5]
	s_waitcnt vmcnt(25)
	v_cvt_pk_bf16_f32 v4, v28, v29
	v_cvt_pk_bf16_f32 v5, v30, v31
	ds_write_b64 v6, v[4:5] offset:26112
	v_add_u32_e32 v4, 0xe00, v0
	v_lshrrev_b32_e32 v7, 6, v4
	s_waitcnt vmcnt(24)
	v_cvt_pk_bf16_f32 v4, v98, v99
	v_cvt_pk_bf16_f32 v5, v100, v101
	v_mad_u32_u24 v7, v7, s6, v1
	ds_write_b64 v7, v[4:5]
	s_waitcnt vmcnt(23)
	v_cvt_pk_bf16_f32 v4, v102, v103
	v_cvt_pk_bf16_f32 v5, v104, v105
	ds_write_b64 v6, v[4:5] offset:34816
	v_add_u32_e32 v4, 0x1200, v0
	v_lshrrev_b32_e32 v7, 6, v4
	s_waitcnt vmcnt(22)
	v_cvt_pk_bf16_f32 v4, v106, v107
	v_cvt_pk_bf16_f32 v5, v108, v109
	v_mad_u32_u24 v7, v7, s6, v1
	ds_write_b64 v7, v[4:5]
	s_waitcnt vmcnt(21)
	v_cvt_pk_bf16_f32 v4, v110, v111
	v_cvt_pk_bf16_f32 v5, v112, v113
	ds_write_b64 v6, v[4:5] offset:43520
	v_add_u32_e32 v4, 0x1600, v0
	v_lshrrev_b32_e32 v7, 6, v4
	s_waitcnt vmcnt(20)
	v_cvt_pk_bf16_f32 v4, v114, v115
	v_cvt_pk_bf16_f32 v5, v116, v117
	v_mad_u32_u24 v7, v7, s6, v1
	ds_write_b64 v7, v[4:5]
	s_waitcnt vmcnt(19)
	v_cvt_pk_bf16_f32 v4, v118, v119
	v_cvt_pk_bf16_f32 v5, v120, v121
	ds_write_b64 v6, v[4:5] offset:52224
	v_add_u32_e32 v4, 0x1a00, v0
	v_lshrrev_b32_e32 v7, 6, v4
	s_waitcnt vmcnt(18)
	v_cvt_pk_bf16_f32 v4, v122, v123
	v_cvt_pk_bf16_f32 v5, v124, v125
	v_mad_u32_u24 v7, v7, s6, v1
	ds_write_b64 v7, v[4:5]
	s_waitcnt vmcnt(17)
	v_cvt_pk_bf16_f32 v4, v126, v127
	v_cvt_pk_bf16_f32 v5, v128, v129
	ds_write_b64 v6, v[4:5] offset:60928
	v_add_u32_e32 v4, 0x1e00, v0
	v_lshrrev_b32_e32 v6, 6, v4
	s_waitcnt vmcnt(16)
	v_cvt_pk_bf16_f32 v4, v132, v133
	v_cvt_pk_bf16_f32 v5, v134, v135
	v_mad_u32_u24 v1, v6, s6, v1
	ds_write_b64 v1, v[4:5]
	s_and_saveexec_b64 s[6:7], s[10:11]
	s_cbranch_execz .LBB0_4
	v_add_u32_e32 v5, 0x22000, v130
	v_add_u32_e32 v6, 0x22200, v130
	v_mul_f32_e32 v1, 0x4038aa3b, v248
	ds_write_b32 v5, v1
	ds_write_b32 v6, v249
